# attention PV: all 9 ds_reads per dt issued ahead, cross-dt LDS read pipelining with separate acc regs
# baseline (speedup 1.0000x reference)
; #define LAS __attribute__((address_space(3)))
; __device__ __forceinline__ void ph_attn_mfma(const Frame& F) {
;     ...
;         f32x4 sacc[9];
; #pragma unroll
;         for (int kt = 0; kt < 9; ++kt) {
;             sacc[kt] = (f32x4){0.f, 0.f, 0.f, 0.f};
;             const LAS unsigned char* kr = lds + AT_K_OFF + ((16 * (wave + kt) + l15) ^ (px << 7)) * AT_KROW + 16 * g;
; #pragma unroll
;             for (int st = 0; st < 4; ++st) {
;                 const bf16x8 af = *(const LAS bf16x8*)(kr + 64 * st);
;                 sacc[kt] = __builtin_amdgcn_mfma_f32_16x16x32_bf16(af, __builtin_bit_cast(bf16x8, qf[st]), sacc[kt], 0, 0, 0);
;             }
;         }
.Lq_skip:
	v_lshl_add_u32 v0, s37, 7, v123
	v_lshlrev_b32_e32 v0, s17, v0
	v_add_u32_e32 v2, s92, v0
	v_xor_b32_e32 v0, s15, v123
	s_movk_i32 s4, 0x110
	v_mad_u64_u32 v[92:93], s[2:3], v0, s4, v[126:127]
	ds_read_b128 v[84:87], v92
	ds_read_b128 v[88:91], v92 offset:64
	v_xor_b32_e32 v0, s15, v156
	s_cmp_lg_u32 s37, 0
	s_cselect_b64 s[22:23], -1, 0
	s_ashr_i32 s17, s16, 31
	s_waitcnt lgkmcnt(1)
	v_mfma_f32_16x16x32_bf16 v[84:87], v[84:87], v[60:63], 0
	s_waitcnt lgkmcnt(0)
	v_mfma_f32_16x16x32_bf16 v[84:87], v[88:91], v[52:55], v[84:87]
	ds_read_b128 v[88:91], v92 offset:128
	s_waitcnt lgkmcnt(0)
	v_mfma_f32_16x16x32_bf16 v[84:87], v[88:91], v[56:59], v[84:87]
	ds_read_b128 v[88:91], v92 offset:192
	v_mad_u64_u32 v[92:93], s[2:3], v0, s4, v[126:127]
	v_xor_b32_e32 v0, s15, v157
	s_waitcnt lgkmcnt(0)
	v_mfma_f32_16x16x32_bf16 v[116:119], v[88:91], v[64:67], v[84:87]
	s_nop 2
	ds_read_b128 v[84:87], v92
	ds_read_b128 v[88:91], v92 offset:64
	s_waitcnt lgkmcnt(1)
	v_mfma_f32_16x16x32_bf16 v[84:87], v[84:87], v[60:63], 0
	s_waitcnt lgkmcnt(0)
	v_mfma_f32_16x16x32_bf16 v[84:87], v[88:91], v[52:55], v[84:87]
	ds_read_b128 v[88:91], v92 offset:128
	s_waitcnt lgkmcnt(0)
	v_mfma_f32_16x16x32_bf16 v[84:87], v[88:91], v[56:59], v[84:87]
	ds_read_b128 v[88:91], v92 offset:192
	v_mad_u64_u32 v[92:93], s[2:3], v0, s4, v[126:127]
	s_waitcnt lgkmcnt(0)
	v_mfma_f32_16x16x32_bf16 v[112:115], v[88:91], v[64:67], v[84:87]
	s_nop 3
	ds_read_b128 v[84:87], v92
	ds_read_b128 v[88:91], v92 offset:64
	v_xor_b32_e32 v0, s15, v158
	s_waitcnt lgkmcnt(1)
	v_mfma_f32_16x16x32_bf16 v[84:87], v[84:87], v[60:63], 0
	v_mul_f32_e32 v112, 0x3e0293ee, v112
	v_mul_f32_e32 v113, 0x3e0293ee, v113
	v_mul_f32_e32 v114, 0x3e0293ee, v114
	s_waitcnt lgkmcnt(0)
	v_mfma_f32_16x16x32_bf16 v[84:87], v[88:91], v[52:55], v[84:87]
	ds_read_b128 v[88:91], v92 offset:128
	v_mul_f32_e32 v115, 0x3e0293ee, v115
	s_waitcnt lgkmcnt(0)
	v_mfma_f32_16x16x32_bf16 v[84:87], v[88:91], v[56:59], v[84:87]
	ds_read_b128 v[88:91], v92 offset:192
	v_mad_u64_u32 v[92:93], s[2:3], v0, s4, v[126:127]
	s_waitcnt lgkmcnt(0)
	v_mfma_f32_16x16x32_bf16 v[108:111], v[88:91], v[64:67], v[84:87]
	s_nop 3
	ds_read_b128 v[84:87], v92
	ds_read_b128 v[88:91], v92 offset:64
	v_xor_b32_e32 v0, s15, v159
	s_waitcnt lgkmcnt(1)
	v_mfma_f32_16x16x32_bf16 v[84:87], v[84:87], v[60:63], 0
	v_mul_f32_e32 v108, 0x3e0293ee, v108
	v_mul_f32_e32 v109, 0x3e0293ee, v109
	v_mul_f32_e32 v110, 0x3e0293ee, v110
	s_waitcnt lgkmcnt(0)
	v_mfma_f32_16x16x32_bf16 v[84:87], v[88:91], v[52:55], v[84:87]
	ds_read_b128 v[88:91], v92 offset:128
	v_mul_f32_e32 v111, 0x3e0293ee, v111
	s_waitcnt lgkmcnt(0)
	v_mfma_f32_16x16x32_bf16 v[84:87], v[88:91], v[56:59], v[84:87]
	ds_read_b128 v[88:91], v92 offset:192
	v_mad_u64_u32 v[92:93], s[2:3], v0, s4, v[126:127]
	s_waitcnt lgkmcnt(0)
	v_mfma_f32_16x16x32_bf16 v[104:107], v[88:91], v[64:67], v[84:87]
	s_nop 3
	ds_read_b128 v[84:87], v92
	ds_read_b128 v[88:91], v92 offset:64
	v_xor_b32_e32 v0, s15, v160
	s_waitcnt lgkmcnt(1)
	v_mfma_f32_16x16x32_bf16 v[84:87], v[84:87], v[60:63], 0
	v_mul_f32_e32 v104, 0x3e0293ee, v104
	v_mul_f32_e32 v105, 0x3e0293ee, v105
	v_mul_f32_e32 v106, 0x3e0293ee, v106
	s_waitcnt lgkmcnt(0)
	v_mfma_f32_16x16x32_bf16 v[84:87], v[88:91], v[52:55], v[84:87]
	ds_read_b128 v[88:91], v92 offset:128
	v_mul_f32_e32 v107, 0x3e0293ee, v107
	s_waitcnt lgkmcnt(0)
	v_mfma_f32_16x16x32_bf16 v[84:87], v[88:91], v[56:59], v[84:87]
	ds_read_b128 v[88:91], v92 offset:192
	v_mad_u64_u32 v[92:93], s[2:3], v0, s4, v[126:127]
	s_waitcnt lgkmcnt(0)
	v_mfma_f32_16x16x32_bf16 v[100:103], v[88:91], v[64:67], v[84:87]
	s_nop 3
	ds_read_b128 v[84:87], v92
	ds_read_b128 v[88:91], v92 offset:64
	v_xor_b32_e32 v0, s15, v161
	s_waitcnt lgkmcnt(1)
	v_mfma_f32_16x16x32_bf16 v[84:87], v[84:87], v[60:63], 0
	v_mul_f32_e32 v100, 0x3e0293ee, v100
	v_mul_f32_e32 v101, 0x3e0293ee, v101
	v_mul_f32_e32 v102, 0x3e0293ee, v102
	s_waitcnt lgkmcnt(0)
	v_mfma_f32_16x16x32_bf16 v[84:87], v[88:91], v[52:55], v[84:87]
	ds_read_b128 v[88:91], v92 offset:128
	v_mul_f32_e32 v103, 0x3e0293ee, v103
	s_waitcnt lgkmcnt(0)
	v_mfma_f32_16x16x32_bf16 v[84:87], v[88:91], v[56:59], v[84:87]
	ds_read_b128 v[88:91], v92 offset:192
	v_mad_u64_u32 v[92:93], s[2:3], v0, s4, v[126:127]
	s_waitcnt lgkmcnt(0)
	v_mfma_f32_16x16x32_bf16 v[96:99], v[88:91], v[64:67], v[84:87]
	s_nop 3
	ds_read_b128 v[84:87], v92
	ds_read_b128 v[88:91], v92 offset:64
	v_xor_b32_e32 v0, s15, v163
	s_waitcnt lgkmcnt(1)
	v_mfma_f32_16x16x32_bf16 v[84:87], v[84:87], v[60:63], 0
	v_mad_u64_u32 v[164:165], s[2:3], v0, s4, v[126:127]
	v_xor_b32_e32 v0, s15, v170
	s_waitcnt lgkmcnt(0)
	v_mfma_f32_16x16x32_bf16 v[84:87], v[88:91], v[52:55], v[84:87]
	ds_read_b128 v[88:91], v92 offset:128
	v_mad_u64_u32 v[180:181], s[2:3], v0, s4, v[126:127]
	s_waitcnt lgkmcnt(0)
	v_mfma_f32_16x16x32_bf16 v[84:87], v[88:91], v[56:59], v[84:87]
	ds_read_b128 v[88:91], v92 offset:192
	v_readlane_b32 s2, v255, 7
	v_readlane_b32 s3, v255, 8
	s_waitcnt lgkmcnt(0)
	v_mfma_f32_16x16x32_bf16 v[92:95], v[88:91], v[64:67], v[84:87]
	s_nop 2
	ds_read_b128 v[84:87], v164
	ds_read_b128 v[88:91], v164 offset:64
	v_readlane_b32 s4, v255, 5
	s_waitcnt lgkmcnt(1)
	v_mfma_f32_16x16x32_bf16 v[84:87], v[84:87], v[60:63], 0
	s_or_b64 s[2:3], s[22:23], s[2:3]
	v_readlane_b32 s5, v255, 6
	s_and_b64 vcc, s[4:5], s[2:3]
	v_readlane_b32 s2, v255, 11
	s_waitcnt lgkmcnt(0)
; #define LAS __attribute__((address_space(3)))
; __device__ __forceinline__ void ph_attn_mfma(const Frame& F) {
;     ...
;         for (int kt = 0; kt < 9; ++kt) {
;             sacc[kt] = (f32x4){0.f, 0.f, 0.f, 0.f};
;             const LAS unsigned char* kr = lds + AT_K_OFF + ((16 * (wave + kt) + l15) ^ (px << 7)) * AT_KROW + 16 * g;
; #pragma unroll
;             for (int st = 0; st < 4; ++st) {
;                 const bf16x8 af = *(const LAS bf16x8*)(kr + 64 * st);
;                 sacc[kt] = __builtin_amdgcn_mfma_f32_16x16x32_bf16(af, __builtin_bit_cast(bf16x8, qf[st]), sacc[kt], 0, 0, 0);
;             }
;         }
;         float mx = -INFINITY;
; #pragma unroll
;         for (int kt = 0; kt < 9; ++kt)
; #pragma unroll
;             for (int i = 0; i < 4; ++i) {
;                 const int rel = 16 * kt + 4 * g + i - l15;
;                 const bool ok = (rel >= 0) && (rel <= 128) && (blk > 0 || (16 * (wave + kt) + 4 * g + i) >= 128);
;                 const float v = ok ? sacc[kt][i] * sc2 : -INFINITY;
;                 sacc[kt][i] = v; mx = fmaxf(mx, v);
;             }
	v_mfma_f32_16x16x32_bf16 v[84:87], v[88:91], v[52:55], v[84:87]
	ds_read_b128 v[88:91], v164 offset:128
	v_readlane_b32 s3, v255, 12
	v_readlane_b32 s4, v255, 9
	v_mul_f32_e32 v0, 0x3e0293ee, v116
	s_or_b64 s[2:3], s[22:23], s[2:3]
	v_readlane_b32 s5, v255, 10
	v_cndmask_b32_e32 v3, v210, v0, vcc
	s_and_b64 vcc, s[4:5], s[2:3]
	v_mul_f32_e32 v0, 0x3e0293ee, v117
	v_cndmask_b32_e32 v116, v210, v0, vcc
	s_mov_b32 s2, 0xff800000
	v_max3_f32 v0, v3, s2, v116
	v_readlane_b32 s2, v255, 15
	v_readlane_b32 s3, v255, 16
	v_readlane_b32 s4, v255, 13
	s_or_b64 s[2:3], s[22:23], s[2:3]
	v_readlane_b32 s5, v255, 14
	s_and_b64 vcc, s[4:5], s[2:3]
	v_readlane_b32 s2, v255, 19
	v_readlane_b32 s3, v255, 20
	v_readlane_b32 s4, v255, 17
	s_waitcnt lgkmcnt(0)
	v_mfma_f32_16x16x32_bf16 v[84:87], v[88:91], v[56:59], v[84:87]
	ds_read_b128 v[88:91], v164 offset:192
	v_mul_f32_e32 v117, 0x3e0293ee, v118
	s_or_b64 s[2:3], s[22:23], s[2:3]
	v_readlane_b32 s5, v255, 18
	v_cndmask_b32_e32 v117, v210, v117, vcc
	s_and_b64 vcc, s[4:5], s[2:3]
	v_readlane_b32 s2, v255, 21
	v_mul_f32_e32 v118, 0x3e0293ee, v119
	v_readlane_b32 s3, v255, 22
	v_cndmask_b32_e32 v118, v210, v118, vcc
	s_or_b64 vcc, s[22:23], s[2:3]
	v_readlane_b32 s2, v255, 23
	v_readlane_b32 s3, v255, 24
	v_cndmask_b32_e32 v112, v210, v112, vcc
	s_or_b64 vcc, s[22:23], s[2:3]
	v_readlane_b32 s2, v255, 25
	v_readlane_b32 s3, v255, 26
	v_cndmask_b32_e32 v113, v210, v113, vcc
	s_or_b64 vcc, s[22:23], s[2:3]
	v_readlane_b32 s2, v255, 27
	v_readlane_b32 s3, v255, 28
	s_waitcnt lgkmcnt(0)
	v_mfma_f32_16x16x32_bf16 v[88:91], v[88:91], v[64:67], v[84:87]
	v_cndmask_b32_e32 v114, v210, v114, vcc
	s_or_b64 vcc, s[22:23], s[2:3]
	v_readlane_b32 s2, v255, 29
	ds_read_b128 v[84:87], v180
	ds_read_b128 v[164:167], v180 offset:64
	v_readlane_b32 s3, v255, 30
	v_cndmask_b32_e32 v115, v210, v115, vcc
	s_or_b64 vcc, s[22:23], s[2:3]
	v_readlane_b32 s2, v255, 31
	v_readlane_b32 s3, v255, 32
	v_cndmask_b32_e32 v108, v210, v108, vcc
	s_or_b64 vcc, s[22:23], s[2:3]
	v_readlane_b32 s2, v255, 33
	v_readlane_b32 s3, v255, 34
	v_cndmask_b32_e32 v109, v210, v109, vcc
	s_or_b64 vcc, s[22:23], s[2:3]
	v_readlane_b32 s2, v255, 35
	v_readlane_b32 s3, v255, 36
	v_cndmask_b32_e32 v110, v210, v110, vcc
	s_or_b64 vcc, s[22:23], s[2:3]
	v_readlane_b32 s2, v255, 37
	s_waitcnt lgkmcnt(1)
	v_mfma_f32_16x16x32_bf16 v[84:87], v[84:87], v[60:63], 0
	v_readlane_b32 s3, v255, 38
	v_cndmask_b32_e32 v111, v210, v111, vcc
	s_or_b64 vcc, s[22:23], s[2:3]
	v_readlane_b32 s2, v255, 39
	v_readlane_b32 s3, v255, 40
	v_cndmask_b32_e32 v104, v210, v104, vcc
	s_or_b64 vcc, s[22:23], s[2:3]
	v_readlane_b32 s2, v255, 41
	s_waitcnt lgkmcnt(0)
	v_mfma_f32_16x16x32_bf16 v[84:87], v[164:167], v[52:55], v[84:87]
	ds_read_b128 v[164:167], v180 offset:128
	v_readlane_b32 s3, v255, 42
	v_cndmask_b32_e32 v105, v210, v105, vcc
	s_or_b64 vcc, s[22:23], s[2:3]
	v_readlane_b32 s2, v255, 43
	v_readlane_b32 s3, v255, 44
	v_cndmask_b32_e32 v106, v210, v106, vcc
	s_or_b64 vcc, s[22:23], s[2:3]
	v_readlane_b32 s2, v255, 45
	v_readlane_b32 s3, v255, 46
	v_cndmask_b32_e32 v107, v210, v107, vcc
	s_or_b64 vcc, s[22:23], s[2:3]
	v_readlane_b32 s2, v255, 47
	v_readlane_b32 s3, v255, 48
	v_cndmask_b32_e32 v100, v210, v100, vcc
	s_or_b64 vcc, s[22:23], s[2:3]
	v_cndmask_b32_e32 v101, v210, v101, vcc
	s_or_b64 vcc, s[22:23], s[48:49]
	s_waitcnt lgkmcnt(0)
	v_mfma_f32_16x16x32_bf16 v[84:87], v[164:167], v[56:59], v[84:87]
	ds_read_b128 v[164:167], v180 offset:192
	v_cndmask_b32_e32 v102, v210, v102, vcc
	s_or_b64 vcc, s[22:23], s[50:51]
	v_cndmask_b32_e32 v103, v210, v103, vcc
	s_or_b64 vcc, s[22:23], s[52:53]
	v_mul_f32_e32 v96, 0x3e0293ee, v96
	v_max3_f32 v0, v0, v117, v118
	v_cndmask_b32_e32 v96, v210, v96, vcc
	s_or_b64 vcc, s[22:23], s[54:55]
	v_mul_f32_e32 v97, 0x3e0293ee, v97
	v_max3_f32 v0, v0, v112, v113
	v_cndmask_b32_e32 v97, v210, v97, vcc
	s_or_b64 vcc, s[22:23], s[56:57]
	v_mul_f32_e32 v98, 0x3e0293ee, v98
	v_max3_f32 v0, v0, v114, v115
	v_cndmask_b32_e32 v98, v210, v98, vcc
	s_or_b64 vcc, s[22:23], s[6:7]
	v_mul_f32_e32 v99, 0x3e0293ee, v99
	v_max3_f32 v0, v0, v108, v109
	v_cndmask_b32_e32 v99, v210, v99, vcc
	s_or_b64 vcc, s[22:23], s[8:9]
	v_mul_f32_e32 v92, 0x3e0293ee, v92
	v_max3_f32 v0, v0, v110, v111
	v_cndmask_b32_e32 v92, v210, v92, vcc
	s_or_b64 vcc, s[22:23], s[62:63]
	v_mul_f32_e32 v93, 0x3e0293ee, v93
	v_max3_f32 v0, v0, v104, v105
	v_cndmask_b32_e32 v93, v210, v93, vcc
	s_or_b64 vcc, s[22:23], s[26:27]
	v_mul_f32_e32 v94, 0x3e0293ee, v94
	v_max3_f32 v0, v0, v106, v107
	v_cndmask_b32_e32 v94, v210, v94, vcc
	s_or_b64 vcc, s[22:23], s[28:29]
	v_mul_f32_e32 v95, 0x3e0293ee, v95
	s_waitcnt lgkmcnt(0)
; __device__ __forceinline__ unsigned pk2(float lo, float hi) { return __builtin_amdgcn_perm(__builtin_bit_cast(unsigned, hi) + 0x8000u, __builtin_bit_cast(unsigned, lo) + 0x8000u, 0x07060302u); }
; __device__ __forceinline__ void ph_attn_mfma(const Frame& F) {
;     ...
;         float mx = -INFINITY;
; #pragma unroll
;         for (int kt = 0; kt < 9; ++kt)
; #pragma unroll
;             for (int i = 0; i < 4; ++i) {
;                 const int rel = 16 * kt + 4 * g + i - l15;
;                 const bool ok = (rel >= 0) && (rel <= 128) && (blk > 0 || (16 * (wave + kt) + 4 * g + i) >= 128);
;                 const float v = ok ? sacc[kt][i] * sc2 : -INFINITY;
;                 sacc[kt][i] = v; mx = fmaxf(mx, v);
;             }
;         mx = xrow_max(mx);
;         float sum = 0.f;
; #pragma unroll
;         for (int kt = 0; kt < 9; ++kt)
; #pragma unroll
;             for (int i = 0; i < 4; ++i) { const float p = __builtin_amdgcn_exp2f(sacc[kt][i] - mx); sacc[kt][i] = p; sum += p; }
;         sum = xrow_sum(sum);
;         v4u pf[5];
; #pragma unroll
;         for (int m = 0; m < 5; ++m) {
;             pf[m].x = pk2(sacc[2 * m][0], sacc[2 * m][1]); pf[m].y = pk2(sacc[2 * m][2], sacc[2 * m][3]);
;             if (m < 4) { pf[m].z = pk2(sacc[2 * m + 1][0], sacc[2 * m + 1][1]); pf[m].w = pk2(sacc[2 * m + 1][2], sacc[2 * m + 1][3]); } else { pf[m].z = 0u; pf[m].w = 0u; }
;         }
	v_mfma_f32_16x16x32_bf16 v[84:87], v[164:167], v[64:67], v[84:87]
	v_max3_f32 v0, v0, v100, v101
	v_cndmask_b32_e32 v95, v210, v95, vcc
	s_or_b64 vcc, s[22:23], s[0:1]
	v_mul_f32_e32 v88, 0x3e0293ee, v88
	v_max3_f32 v0, v0, v102, v103
	v_cndmask_b32_e32 v88, v210, v88, vcc
	s_or_b64 vcc, s[22:23], s[70:71]
	v_mul_f32_e32 v89, 0x3e0293ee, v89
	v_max3_f32 v0, v0, v96, v97
	v_cndmask_b32_e32 v89, v210, v89, vcc
	s_or_b64 vcc, s[22:23], s[72:73]
	v_mul_f32_e32 v90, 0x3e0293ee, v90
	v_max3_f32 v0, v0, v98, v99
	v_cndmask_b32_e32 v90, v210, v90, vcc
	s_or_b64 vcc, s[22:23], s[74:75]
	v_mul_f32_e32 v91, 0x3e0293ee, v91
	s_or_b64 s[2:3], s[22:23], s[78:79]
	v_max3_f32 v0, v0, v92, v93
	v_cndmask_b32_e32 v91, v210, v91, vcc
	s_and_b64 vcc, s[76:77], s[2:3]
	v_mul_f32_e32 v84, 0x3e0293ee, v84
	s_or_b64 s[2:3], s[22:23], s[82:83]
	v_max3_f32 v0, v0, v94, v95
	v_cndmask_b32_e32 v84, v210, v84, vcc
	s_and_b64 vcc, s[80:81], s[2:3]
	v_mul_f32_e32 v85, 0x3e0293ee, v85
	s_or_b64 s[2:3], s[22:23], s[86:87]
	v_max3_f32 v0, v0, v88, v89
	v_cndmask_b32_e32 v85, v210, v85, vcc
	s_and_b64 vcc, s[84:85], s[2:3]
	v_mul_f32_e32 v86, 0x3e0293ee, v86
	s_or_b64 s[2:3], s[22:23], s[90:91]
	v_max3_f32 v0, v0, v90, v91
	v_cndmask_b32_e32 v86, v210, v86, vcc
	s_and_b64 vcc, s[88:89], s[2:3]
	v_mul_f32_e32 v87, 0x3e0293ee, v87
	v_max3_f32 v0, v0, v84, v85
	v_cndmask_b32_e32 v87, v210, v87, vcc
	v_max3_f32 v0, v0, v86, v87
	v_mov_b32_e32 v119, v0
	s_nop 1
	v_permlane16_swap_b32_e32 v0, v119
	v_max_f32_e32 v119, v119, v119
	v_max_f32_e32 v0, v0, v0
	v_max_f32_e32 v0, v0, v119
	v_mov_b32_e32 v119, v0
	s_nop 1
	v_permlane32_swap_b32_e32 v0, v119
	v_max_f32_e32 v119, v119, v119
	v_max_f32_e32 v0, v0, v0
	v_max_f32_e32 v0, v0, v119
	v_sub_f32_e32 v3, v3, v0
	v_exp_f32_e32 v3, v3
	v_sub_f32_e32 v116, v116, v0
	v_exp_f32_e32 v116, v116
	v_sub_f32_e32 v117, v117, v0
	v_exp_f32_e32 v117, v117
	v_sub_f32_e32 v118, v118, v0
	v_exp_f32_e32 v118, v118
	v_sub_f32_e32 v112, v112, v0
	v_add_f32_e32 v119, 0, v3
	v_exp_f32_e32 v112, v112
	v_sub_f32_e32 v113, v113, v0
	v_add_f32_e32 v119, v116, v119
	v_exp_f32_e32 v113, v113
	v_sub_f32_e32 v114, v114, v0
	v_add_f32_e32 v119, v117, v119
	v_exp_f32_e32 v114, v114
	v_sub_f32_e32 v115, v115, v0
	v_add_f32_e32 v119, v118, v119
	v_exp_f32_e32 v115, v115
	v_sub_f32_e32 v108, v108, v0
	v_add_f32_e32 v119, v112, v119
	v_exp_f32_e32 v108, v108
	v_sub_f32_e32 v109, v109, v0
	v_add_f32_e32 v119, v113, v119
	v_exp_f32_e32 v109, v109
	v_sub_f32_e32 v110, v110, v0
	v_add_f32_e32 v119, v114, v119
	v_exp_f32_e32 v110, v110
	v_sub_f32_e32 v111, v111, v0
	v_add_f32_e32 v119, v115, v119
	v_exp_f32_e32 v111, v111
	v_sub_f32_e32 v104, v104, v0
	v_add_f32_e32 v119, v108, v119
	v_exp_f32_e32 v104, v104
	v_sub_f32_e32 v105, v105, v0
	v_add_f32_e32 v119, v109, v119
	v_exp_f32_e32 v105, v105
	v_sub_f32_e32 v106, v106, v0
	v_add_f32_e32 v119, v110, v119
	v_exp_f32_e32 v106, v106
	v_sub_f32_e32 v107, v107, v0
	v_add_f32_e32 v119, v111, v119
	v_exp_f32_e32 v107, v107
	v_sub_f32_e32 v100, v100, v0
	v_add_f32_e32 v119, v104, v119
	v_exp_f32_e32 v129, v100
	v_add_f32_e32 v119, v105, v119
	v_add_f32_e32 v119, v106, v119
	v_add_f32_e32 v119, v107, v119
	v_sub_f32_e32 v101, v101, v0
	v_add_f32_e32 v100, v129, v119
	v_exp_f32_e32 v119, v101
	v_sub_f32_e32 v101, v102, v0
	v_exp_f32_e32 v131, v101
	v_sub_f32_e32 v101, v103, v0
	v_exp_f32_e32 v164, v101
	v_sub_f32_e32 v96, v96, v0
	v_exp_f32_e32 v165, v96
	v_sub_f32_e32 v97, v97, v0
	v_add_f32_e32 v100, v119, v100
	v_exp_f32_e32 v166, v97
	v_sub_f32_e32 v97, v98, v0
	v_add_f32_e32 v100, v131, v100
	v_exp_f32_e32 v167, v97
	v_sub_f32_e32 v97, v99, v0
	v_add_f32_e32 v100, v164, v100
	v_exp_f32_e32 v180, v97
	v_sub_f32_e32 v92, v92, v0
	v_add_f32_e32 v96, v165, v100
	v_exp_f32_e32 v92, v92
	v_sub_f32_e32 v93, v93, v0
	v_add_f32_e32 v96, v166, v96
	v_exp_f32_e32 v93, v93
	v_sub_f32_e32 v94, v94, v0
	v_add_f32_e32 v96, v167, v96
	v_exp_f32_e32 v94, v94
	v_sub_f32_e32 v95, v95, v0
	v_add_f32_e32 v96, v180, v96
	v_exp_f32_e32 v95, v95
	v_sub_f32_e32 v88, v88, v0
	v_add_f32_e32 v96, v92, v96
	v_exp_f32_e32 v181, v88
	v_sub_f32_e32 v89, v89, v0
	v_add_f32_e32 v96, v93, v96
	v_exp_f32_e32 v182, v89
	v_sub_f32_e32 v89, v90, v0
	v_add_f32_e32 v96, v94, v96
	v_exp_f32_e32 v183, v89
	v_sub_f32_e32 v89, v91, v0
	v_add_f32_e32 v96, v95, v96
	v_exp_f32_e32 v184, v89
	v_sub_f32_e32 v84, v84, v0
	v_add_f32_e32 v88, v181, v96
	v_exp_f32_e32 v84, v84
	v_sub_f32_e32 v85, v85, v0
	v_add_f32_e32 v88, v182, v88
	v_exp_f32_e32 v85, v85
	v_sub_f32_e32 v86, v86, v0
	v_add_f32_e32 v88, v183, v88
	v_exp_f32_e32 v86, v86
	v_sub_f32_e32 v87, v87, v0
	v_add_f32_e32 v88, v184, v88
	v_exp_f32_e32 v87, v87
	v_add_f32_e32 v88, v84, v88
	v_add_f32_e32 v88, v85, v88
	v_add_f32_e32 v88, v86, v88
	v_add_f32_e32 v88, v87, v88
	v_mov_b32_e32 v89, v88
	s_nop 1
	v_permlane16_swap_b32_e32 v88, v89
	v_add_f32_e32 v185, v88, v89
	v_add_u32_e32 v88, 0x8000, v116
	v_add_u32_e32 v3, 0x8000, v3
	v_perm_b32 v100, v88, v3, s33
	v_add_u32_e32 v3, 0x8000, v118
	v_add_u32_e32 v88, 0x8000, v117
	v_perm_b32 v101, v3, v88, s33
	v_add_u32_e32 v3, 0x8000, v113
	v_add_u32_e32 v88, 0x8000, v112
	v_perm_b32 v102, v3, v88, s33
	v_add_u32_e32 v3, 0x8000, v115
	v_add_u32_e32 v88, 0x8000, v114
	v_perm_b32 v103, v3, v88, s33
	v_add_u32_e32 v3, 0x8000, v109
	v_add_u32_e32 v88, 0x8000, v108
	v_perm_b32 v96, v3, v88, s33
	v_add_u32_e32 v3, 0x8000, v111
	v_add_u32_e32 v88, 0x8000, v110
	v_perm_b32 v97, v3, v88, s33
	v_add_u32_e32 v3, 0x8000, v105
	v_add_u32_e32 v88, 0x8000, v104
	v_perm_b32 v98, v3, v88, s33
	v_add_u32_e32 v3, 0x8000, v107
	v_add_u32_e32 v88, 0x8000, v106
	v_perm_b32 v99, v3, v88, s33
; #define LAS __attribute__((address_space(3)))
; __device__ __forceinline__ unsigned pk2(float lo, float hi) { return __builtin_amdgcn_perm(__builtin_bit_cast(unsigned, hi) + 0x8000u, __builtin_bit_cast(unsigned, lo) + 0x8000u, 0x07060302u); }
; __device__ __forceinline__ void ph_attn_mfma(const Frame& F) {
;     ...
;         v4u pf[5];
; #pragma unroll
;         for (int m = 0; m < 5; ++m) {
;             pf[m].x = pk2(sacc[2 * m][0], sacc[2 * m][1]); pf[m].y = pk2(sacc[2 * m][2], sacc[2 * m][3]);
;             if (m < 4) { pf[m].z = pk2(sacc[2 * m + 1][0], sacc[2 * m + 1][1]); pf[m].w = pk2(sacc[2 * m + 1][2], sacc[2 * m + 1][3]); } else { pf[m].z = 0u; pf[m].w = 0u; }
;         }
;         const float rs = 1.0f / sum;
;         bf16* orow = OG + ((size_t)br * T + qtok) * 1024 + hd * 128 + 4 * g;
; #pragma unroll
;         for (int dt = 0; dt < 8; ++dt) {
;             f32x4 o = (f32x4){0.f, 0.f, 0.f, 0.f};
;             const LAS unsigned char* vr = lds + AT_V_OFF + (16 * dt + l15) * AT_VROW;  const int kv0 = 16 * wave + 4 * g;
; #pragma unroll
;             for (int m = 0; m < 5; ++m) {
;                 const v2u p0 = *(const LAS v2u*)(vr + ((kv0 + 32 * m) ^ (px << 7)) * 2);
;                 const v2u p1 = *(const LAS v2u*)(vr + ((kv0 + 32 * m + (m < 4 ? 16 : 0)) ^ (px << 7)) * 2);
;                 const v4u af = (v4u){p0.x, p0.y, p1.x, p1.y};
;                 o = __builtin_amdgcn_mfma_f32_16x16x32_bf16(__builtin_bit_cast(bf16x8, af), __builtin_bit_cast(bf16x8, pf[m]), o, 0, 0, 0);
;             }
;             v2u w; w.x = pk2(o[0] * rs, o[1] * rs); w.y = pk2(o[2] * rs, o[3] * rs);
;             *(v2u*)(orow + 16 * dt) = w;
;         }
	v_add_u32_e32 v3, 0x8000, v119
	v_add_u32_e32 v88, 0x8000, v129
	v_perm_b32 v88, v3, v88, s33
	v_add_u32_e32 v3, 0x8000, v164
	v_add_u32_e32 v89, 0x8000, v131
	v_perm_b32 v89, v3, v89, s33
	v_add_u32_e32 v3, 0x8000, v166
	v_add_u32_e32 v90, 0x8000, v165
	v_perm_b32 v90, v3, v90, s33
	v_add_u32_e32 v3, 0x8000, v180
	v_add_u32_e32 v91, 0x8000, v167
	v_perm_b32 v91, v3, v91, s33
	v_add_u32_e32 v3, 0x8000, v93
	v_add_u32_e32 v92, 0x8000, v92
	v_perm_b32 v92, v3, v92, s33
	v_add_u32_e32 v3, 0x8000, v95
	v_add_u32_e32 v93, 0x8000, v94
	v_perm_b32 v93, v3, v93, s33
	v_add_u32_e32 v3, 0x8000, v182
	v_add_u32_e32 v94, 0x8000, v181
	v_mov_b32_e32 v186, v185
	v_perm_b32 v94, v3, v94, s33
	v_add_u32_e32 v3, 0x8000, v184
	v_add_u32_e32 v95, 0x8000, v183
	v_permlane32_swap_b32_e32 v185, v186
	v_perm_b32 v95, v3, v95, s33
	v_add_u32_e32 v3, 0x8000, v85
	v_add_u32_e32 v84, 0x8000, v84
	v_perm_b32 v84, v3, v84, s33
	v_add_u32_e32 v3, 0x8000, v87
	v_add_u32_e32 v85, 0x8000, v86
	v_add_f32_e32 v110, v185, v186
	v_perm_b32 v85, v3, v85, s33
	v_div_scale_f32 v3, s[2:3], v110, v110, 1.0
	v_rcp_f32_e32 v104, v3
	s_lshl_b64 s[2:3], s[16:17], 14
	v_mov_b32_e32 v129, v1
	v_xor_b32_e32 v112, s15, v173
	v_fma_f32 v105, -v3, v104, 1.0
	v_fmac_f32_e32 v104, v105, v104
	v_div_scale_f32 v105, vcc, 1.0, v110, 1.0
	v_mul_f32_e32 v106, v105, v104
	v_fma_f32 v107, -v3, v106, v105
	v_fmac_f32_e32 v106, v107, v104
	v_fma_f32 v3, -v3, v106, v105
	v_div_fmas_f32 v3, v3, v104, v106
	v_div_fixup_f32 v111, v3, v110, 1.0
	v_ashrrev_i32_e32 v3, 31, v2
	v_lshl_add_u64 v[2:3], s[2:3], 0, v[2:3]
	v_lshlrev_b64 v[104:105], 11, v[2:3]
	s_lshl_b32 s2, s14, 7
	v_lshl_add_u64 v[104:105], s[12:13], 0, v[104:105]
	s_ashr_i32 s3, s2, 31
	v_lshl_add_u64 v[104:105], s[2:3], 1, v[104:105]
	v_lshl_add_u64 v[108:109], v[104:105], 0, v[128:129]
	v_xor_b32_e32 v104, s15, v150
	v_xor_b32_e32 v106, s15, v172
	v_lshl_add_u32 v116, v104, 1, v171
	v_lshl_add_u32 v118, v106, 1, v171
	ds_read_b64 v[104:105], v116
	ds_read_b64 v[106:107], v118
	v_xor_b32_e32 v113, s15, v174
	v_lshl_add_u32 v112, v112, 1, v171
	v_lshl_add_u32 v114, v113, 1, v171
	ds_read_b64 v[164:165], v112
	ds_read_b64 v[166:167], v114
	v_xor_b32_e32 v113, s15, v175
	v_xor_b32_e32 v115, s15, v176
	v_lshl_add_u32 v113, v113, 1, v171
	v_lshl_add_u32 v115, v115, 1, v171
	ds_read_b64 v[236:237], v113
	ds_read_b64 v[238:239], v115
	v_xor_b32_e32 v117, s15, v177
	v_lshl_add_u32 v119, v117, 1, v171
	v_xor_b32_e32 v117, s15, v178
	v_lshl_add_u32 v129, v117, 1, v171
	ds_read_b64 v[240:241], v119
	ds_read_b64 v[242:243], v129
	v_xor_b32_e32 v117, s15, v179
	v_lshl_add_u32 v117, v117, 1, v171
	ds_read_b64 v[244:245], v117
	v_mov_b32_e32 v86, v1
	v_mov_b32_e32 v87, v1
	s_waitcnt lgkmcnt(7)
	v_mfma_f32_16x16x32_bf16 v[248:251], v[104:107], v[100:103], 0
	ds_read_b64 v[104:105], v116 offset:8448
	ds_read_b64 v[106:107], v118 offset:8448
	s_waitcnt lgkmcnt(7)
	v_mfma_f32_16x16x32_bf16 v[248:251], v[164:167], v[96:99], v[248:251]
	ds_read_b64 v[164:165], v112 offset:8448
	ds_read_b64 v[166:167], v114 offset:8448
	s_waitcnt lgkmcnt(7)
	v_mfma_f32_16x16x32_bf16 v[248:251], v[236:239], v[88:91], v[248:251]
	ds_read_b64 v[236:237], v113 offset:8448
	ds_read_b64 v[238:239], v115 offset:8448
	s_waitcnt lgkmcnt(7)
	v_mfma_f32_16x16x32_bf16 v[248:251], v[240:243], v[92:95], v[248:251]
	ds_read_b64 v[240:241], v119 offset:8448
	ds_read_b64 v[242:243], v129 offset:8448
	s_waitcnt lgkmcnt(8)
	v_mov_b32_e32 v246, v244
	v_mov_b32_e32 v247, v245
	s_nop 1
	v_mfma_f32_16x16x32_bf16 v[248:251], v[244:247], v[84:87], v[248:251]
	ds_read_b64 v[244:245], v117 offset:8448
	s_nop 7
	v_mul_f32_e32 v248, v111, v248
	v_mul_f32_e32 v249, v111, v249
	v_add_u32_e32 v249, 0x8000, v249
	v_add_u32_e32 v248, 0x8000, v248
	v_perm_b32 v248, v249, v248, s33
	v_mul_f32_e32 v249, v111, v250
	v_mul_f32_e32 v250, v111, v251
	v_add_u32_e32 v250, 0x8000, v250
	v_add_u32_e32 v249, 0x8000, v249
	v_perm_b32 v249, v250, v249, s33
	global_store_dwordx2 v[108:109], v[248:249], off
	s_waitcnt lgkmcnt(7)
	v_mfma_f32_16x16x32_bf16 v[248:251], v[104:107], v[100:103], 0
	ds_read_b64 v[104:105], v116 offset:16896
	ds_read_b64 v[106:107], v118 offset:16896
	s_waitcnt lgkmcnt(7)
	v_mfma_f32_16x16x32_bf16 v[248:251], v[164:167], v[96:99], v[248:251]
	ds_read_b64 v[164:165], v112 offset:16896
	ds_read_b64 v[166:167], v114 offset:16896
	s_waitcnt lgkmcnt(7)
	v_mfma_f32_16x16x32_bf16 v[248:251], v[236:239], v[88:91], v[248:251]
	ds_read_b64 v[236:237], v113 offset:16896
	ds_read_b64 v[238:239], v115 offset:16896
	s_waitcnt lgkmcnt(7)
	v_mfma_f32_16x16x32_bf16 v[248:251], v[240:243], v[92:95], v[248:251]
	ds_read_b64 v[240:241], v119 offset:16896
	ds_read_b64 v[242:243], v129 offset:16896
	s_waitcnt lgkmcnt(8)
	v_mov_b32_e32 v246, v244
	v_mov_b32_e32 v247, v245
	s_nop 1
	v_mfma_f32_16x16x32_bf16 v[248:251], v[244:247], v[84:87], v[248:251]
	ds_read_b64 v[244:245], v117 offset:16896
	s_nop 7
	v_mul_f32_e32 v248, v111, v248
	v_mul_f32_e32 v249, v111, v249
	v_add_u32_e32 v249, 0x8000, v249
	v_add_u32_e32 v248, 0x8000, v248
	v_perm_b32 v248, v249, v248, s33
	v_mul_f32_e32 v249, v111, v250
	v_mul_f32_e32 v250, v111, v251
	v_add_u32_e32 v250, 0x8000, v250
	v_add_u32_e32 v249, 0x8000, v249
	v_perm_b32 v249, v250, v249, s33
	global_store_dwordx2 v[108:109], v[248:249], off offset:32
	s_waitcnt lgkmcnt(7)
	v_mfma_f32_16x16x32_bf16 v[248:251], v[104:107], v[100:103], 0
	ds_read_b64 v[104:105], v116 offset:25344
	ds_read_b64 v[106:107], v118 offset:25344
	s_waitcnt lgkmcnt(7)
	v_mfma_f32_16x16x32_bf16 v[248:251], v[164:167], v[96:99], v[248:251]
	ds_read_b64 v[164:165], v112 offset:25344
	ds_read_b64 v[166:167], v114 offset:25344
	s_waitcnt lgkmcnt(7)
; #define LAS __attribute__((address_space(3)))
; __device__ __forceinline__ unsigned pk2(float lo, float hi) { return __builtin_amdgcn_perm(__builtin_bit_cast(unsigned, hi) + 0x8000u, __builtin_bit_cast(unsigned, lo) + 0x8000u, 0x07060302u); }
; __device__ __forceinline__ void ph_attn_mfma(const Frame& F) {
;     ...
;         for (int dt = 0; dt < 8; ++dt) {
;             f32x4 o = (f32x4){0.f, 0.f, 0.f, 0.f};
;             const LAS unsigned char* vr = lds + AT_V_OFF + (16 * dt + l15) * AT_VROW;  const int kv0 = 16 * wave + 4 * g;
; #pragma unroll
;             for (int m = 0; m < 5; ++m) {
;                 const v2u p0 = *(const LAS v2u*)(vr + ((kv0 + 32 * m) ^ (px << 7)) * 2);
;                 const v2u p1 = *(const LAS v2u*)(vr + ((kv0 + 32 * m + (m < 4 ? 16 : 0)) ^ (px << 7)) * 2);
;                 const v4u af = (v4u){p0.x, p0.y, p1.x, p1.y};
;                 o = __builtin_amdgcn_mfma_f32_16x16x32_bf16(__builtin_bit_cast(bf16x8, af), __builtin_bit_cast(bf16x8, pf[m]), o, 0, 0, 0);
;             }
;             v2u w; w.x = pk2(o[0] * rs, o[1] * rs); w.y = pk2(o[2] * rs, o[3] * rs);
;             *(v2u*)(orow + 16 * dt) = w;
;         }
	v_mfma_f32_16x16x32_bf16 v[248:251], v[236:239], v[88:91], v[248:251]
	ds_read_b64 v[236:237], v113 offset:25344
	ds_read_b64 v[238:239], v115 offset:25344
	s_waitcnt lgkmcnt(7)
	v_mfma_f32_16x16x32_bf16 v[248:251], v[240:243], v[92:95], v[248:251]
	ds_read_b64 v[240:241], v119 offset:25344
	ds_read_b64 v[242:243], v129 offset:25344
	s_waitcnt lgkmcnt(8)
	v_mov_b32_e32 v246, v244
	v_mov_b32_e32 v247, v245
	s_nop 1
	v_mfma_f32_16x16x32_bf16 v[248:251], v[244:247], v[84:87], v[248:251]
	ds_read_b64 v[244:245], v117 offset:25344
	s_nop 7
	v_mul_f32_e32 v248, v111, v248
	v_mul_f32_e32 v249, v111, v249
	v_add_u32_e32 v249, 0x8000, v249
	v_add_u32_e32 v248, 0x8000, v248
	v_perm_b32 v248, v249, v248, s33
	v_mul_f32_e32 v249, v111, v250
	v_mul_f32_e32 v250, v111, v251
	v_add_u32_e32 v250, 0x8000, v250
	v_add_u32_e32 v249, 0x8000, v249
	v_perm_b32 v249, v250, v249, s33
	global_store_dwordx2 v[108:109], v[248:249], off offset:64
	s_waitcnt lgkmcnt(7)
	v_mfma_f32_16x16x32_bf16 v[248:251], v[104:107], v[100:103], 0
	ds_read_b64 v[104:105], v116 offset:33792
	ds_read_b64 v[106:107], v118 offset:33792
	s_waitcnt lgkmcnt(7)
	v_mfma_f32_16x16x32_bf16 v[248:251], v[164:167], v[96:99], v[248:251]
	ds_read_b64 v[164:165], v112 offset:33792
	ds_read_b64 v[166:167], v114 offset:33792
	s_waitcnt lgkmcnt(7)
	v_mfma_f32_16x16x32_bf16 v[248:251], v[236:239], v[88:91], v[248:251]
	ds_read_b64 v[236:237], v113 offset:33792
	ds_read_b64 v[238:239], v115 offset:33792
	s_waitcnt lgkmcnt(7)
	v_mfma_f32_16x16x32_bf16 v[248:251], v[240:243], v[92:95], v[248:251]
	ds_read_b64 v[240:241], v119 offset:33792
	ds_read_b64 v[242:243], v129 offset:33792
	s_waitcnt lgkmcnt(8)
	v_mov_b32_e32 v246, v244
	v_mov_b32_e32 v247, v245
	s_nop 1
	v_mfma_f32_16x16x32_bf16 v[248:251], v[244:247], v[84:87], v[248:251]
	ds_read_b64 v[244:245], v117 offset:33792
	s_nop 7
	v_mul_f32_e32 v248, v111, v248
	v_mul_f32_e32 v249, v111, v249
	v_add_u32_e32 v249, 0x8000, v249
	v_add_u32_e32 v248, 0x8000, v248
	v_perm_b32 v248, v249, v248, s33
	v_mul_f32_e32 v249, v111, v250
	v_mul_f32_e32 v250, v111, v251
	v_add_u32_e32 v250, 0x8000, v250
	v_add_u32_e32 v249, 0x8000, v249
	v_perm_b32 v249, v250, v249, s33
	global_store_dwordx2 v[108:109], v[248:249], off offset:96
	s_waitcnt lgkmcnt(7)
	v_mfma_f32_16x16x32_bf16 v[248:251], v[104:107], v[100:103], 0
	ds_read_b64 v[104:105], v116 offset:42240
	ds_read_b64 v[106:107], v118 offset:42240
	s_waitcnt lgkmcnt(7)
	v_mfma_f32_16x16x32_bf16 v[248:251], v[164:167], v[96:99], v[248:251]
	ds_read_b64 v[164:165], v112 offset:42240
	ds_read_b64 v[166:167], v114 offset:42240
	s_waitcnt lgkmcnt(7)
	v_mfma_f32_16x16x32_bf16 v[248:251], v[236:239], v[88:91], v[248:251]
	ds_read_b64 v[236:237], v113 offset:42240
	ds_read_b64 v[238:239], v115 offset:42240
	s_waitcnt lgkmcnt(7)
	v_mfma_f32_16x16x32_bf16 v[248:251], v[240:243], v[92:95], v[248:251]
	ds_read_b64 v[240:241], v119 offset:42240
	ds_read_b64 v[242:243], v129 offset:42240
	s_waitcnt lgkmcnt(8)
	v_mov_b32_e32 v246, v244
	v_mov_b32_e32 v247, v245
	s_nop 1
	v_mfma_f32_16x16x32_bf16 v[248:251], v[244:247], v[84:87], v[248:251]
	ds_read_b64 v[244:245], v117 offset:42240
	s_nop 7
	v_mul_f32_e32 v248, v111, v248
	v_mul_f32_e32 v249, v111, v249
	v_add_u32_e32 v249, 0x8000, v249
	v_add_u32_e32 v248, 0x8000, v248
	v_perm_b32 v248, v249, v248, s33
	v_mul_f32_e32 v249, v111, v250
	v_mul_f32_e32 v250, v111, v251
	v_add_u32_e32 v250, 0x8000, v250
	v_add_u32_e32 v249, 0x8000, v249
	v_perm_b32 v249, v250, v249, s33
	global_store_dwordx2 v[108:109], v[248:249], off offset:128
	s_waitcnt lgkmcnt(7)
	v_mfma_f32_16x16x32_bf16 v[248:251], v[104:107], v[100:103], 0
	ds_read_b64 v[104:105], v116 offset:50688
	ds_read_b64 v[106:107], v118 offset:50688
	s_waitcnt lgkmcnt(7)
	v_mfma_f32_16x16x32_bf16 v[248:251], v[164:167], v[96:99], v[248:251]
	ds_read_b64 v[164:165], v112 offset:50688
	ds_read_b64 v[166:167], v114 offset:50688
	s_waitcnt lgkmcnt(7)
; #define LAS __attribute__((address_space(3)))
; __device__ __forceinline__ unsigned pk2(float lo, float hi) { return __builtin_amdgcn_perm(__builtin_bit_cast(unsigned, hi) + 0x8000u, __builtin_bit_cast(unsigned, lo) + 0x8000u, 0x07060302u); }
; __device__ __forceinline__ void ph_attn_mfma(const Frame& F) {
;     ...
;         for (int dt = 0; dt < 8; ++dt) {
;             f32x4 o = (f32x4){0.f, 0.f, 0.f, 0.f};
;             const LAS unsigned char* vr = lds + AT_V_OFF + (16 * dt + l15) * AT_VROW;  const int kv0 = 16 * wave + 4 * g;
; #pragma unroll
;             for (int m = 0; m < 5; ++m) {
;                 const v2u p0 = *(const LAS v2u*)(vr + ((kv0 + 32 * m) ^ (px << 7)) * 2);
;                 const v2u p1 = *(const LAS v2u*)(vr + ((kv0 + 32 * m + (m < 4 ? 16 : 0)) ^ (px << 7)) * 2);
;                 const v4u af = (v4u){p0.x, p0.y, p1.x, p1.y};
;                 o = __builtin_amdgcn_mfma_f32_16x16x32_bf16(__builtin_bit_cast(bf16x8, af), __builtin_bit_cast(bf16x8, pf[m]), o, 0, 0, 0);
;             }
;             v2u w; w.x = pk2(o[0] * rs, o[1] * rs); w.y = pk2(o[2] * rs, o[3] * rs);
;             *(v2u*)(orow + 16 * dt) = w;
;         }
;         if (g == 0) LSE[((size_t)br * T + qtok) * 8 + hd] = mx * 0.6931471805599453f + __logf(sum);
	v_mfma_f32_16x16x32_bf16 v[248:251], v[236:239], v[88:91], v[248:251]
	ds_read_b64 v[236:237], v113 offset:50688
	ds_read_b64 v[238:239], v115 offset:50688
	s_waitcnt lgkmcnt(7)
	v_mfma_f32_16x16x32_bf16 v[248:251], v[240:243], v[92:95], v[248:251]
	ds_read_b64 v[240:241], v119 offset:50688
	ds_read_b64 v[242:243], v129 offset:50688
	s_waitcnt lgkmcnt(8)
	v_mov_b32_e32 v246, v244
	v_mov_b32_e32 v247, v245
	s_nop 1
	v_mfma_f32_16x16x32_bf16 v[248:251], v[244:247], v[84:87], v[248:251]
	ds_read_b64 v[244:245], v117 offset:50688
	s_nop 7
	v_mul_f32_e32 v248, v111, v248
	v_mul_f32_e32 v249, v111, v249
	v_add_u32_e32 v249, 0x8000, v249
	v_add_u32_e32 v248, 0x8000, v248
	v_perm_b32 v248, v249, v248, s33
	v_mul_f32_e32 v249, v111, v250
	v_mul_f32_e32 v250, v111, v251
	v_add_u32_e32 v250, 0x8000, v250
	v_add_u32_e32 v249, 0x8000, v249
	v_perm_b32 v249, v250, v249, s33
	global_store_dwordx2 v[108:109], v[248:249], off offset:160
	s_waitcnt lgkmcnt(7)
	v_mfma_f32_16x16x32_bf16 v[248:251], v[104:107], v[100:103], 0
	ds_read_b64 v[104:105], v116 offset:59136
	ds_read_b64 v[106:107], v118 offset:59136
	s_waitcnt lgkmcnt(7)
	v_mfma_f32_16x16x32_bf16 v[248:251], v[164:167], v[96:99], v[248:251]
	ds_read_b64 v[164:165], v112 offset:59136
	ds_read_b64 v[166:167], v114 offset:59136
	s_waitcnt lgkmcnt(7)
	v_mfma_f32_16x16x32_bf16 v[248:251], v[236:239], v[88:91], v[248:251]
	ds_read_b64 v[236:237], v113 offset:59136
	ds_read_b64 v[238:239], v115 offset:59136
	s_waitcnt lgkmcnt(7)
	v_mfma_f32_16x16x32_bf16 v[248:251], v[240:243], v[92:95], v[248:251]
	ds_read_b64 v[240:241], v119 offset:59136
	ds_read_b64 v[242:243], v129 offset:59136
	s_waitcnt lgkmcnt(8)
	v_mov_b32_e32 v246, v244
	v_mov_b32_e32 v247, v245
	s_nop 1
	v_mfma_f32_16x16x32_bf16 v[248:251], v[244:247], v[84:87], v[248:251]
	ds_read_b64 v[244:245], v117 offset:59136
	s_nop 7
	v_mul_f32_e32 v248, v111, v248
	v_mul_f32_e32 v249, v111, v249
	v_add_u32_e32 v249, 0x8000, v249
	v_add_u32_e32 v248, 0x8000, v248
	v_perm_b32 v248, v249, v248, s33
	v_mul_f32_e32 v249, v111, v250
	v_mul_f32_e32 v250, v111, v251
	v_add_u32_e32 v250, 0x8000, v250
	v_add_u32_e32 v249, 0x8000, v249
	v_perm_b32 v249, v250, v249, s33
	global_store_dwordx2 v[108:109], v[248:249], off offset:192
	s_waitcnt lgkmcnt(7)
	v_mfma_f32_16x16x32_bf16 v[248:251], v[104:107], v[100:103], 0
	s_waitcnt lgkmcnt(5)
	v_mfma_f32_16x16x32_bf16 v[248:251], v[164:167], v[96:99], v[248:251]
	s_waitcnt lgkmcnt(3)
	v_mfma_f32_16x16x32_bf16 v[248:251], v[236:239], v[88:91], v[248:251]
	s_waitcnt lgkmcnt(1)
	v_mfma_f32_16x16x32_bf16 v[248:251], v[240:243], v[92:95], v[248:251]
	s_waitcnt lgkmcnt(0)
	v_mov_b32_e32 v246, v244
	v_mov_b32_e32 v247, v245
	s_nop 1
	v_mfma_f32_16x16x32_bf16 v[248:251], v[244:247], v[84:87], v[248:251]
	s_nop 7
	v_mul_f32_e32 v248, v111, v248
	v_mul_f32_e32 v249, v111, v249
	v_add_u32_e32 v249, 0x8000, v249
	v_add_u32_e32 v248, 0x8000, v248
	v_perm_b32 v248, v249, v248, s33
	v_mul_f32_e32 v249, v111, v250
	v_mul_f32_e32 v250, v111, v251
	v_add_u32_e32 v250, 0x8000, v250
	v_add_u32_e32 v249, 0x8000, v249
	v_perm_b32 v249, v250, v249, s33
	global_store_dwordx2 v[108:109], v[248:249], off offset:224
	s_and_saveexec_b64 s[22:23], s[46:47]
	s_cbranch_execz .LBB0_899
	s_mov_b32 s2, 0x800000
	v_cmp_gt_f32_e32 vcc, s2, v110
	s_mov_b32 s2, 0x3f317217
	v_mov_b32_e32 v85, 0x41b17218
	v_cndmask_b32_e64 v84, 0, 32, vcc
	v_ldexp_f32 v84, v110, v84
	v_log_f32_e32 v84, v84
	v_cndmask_b32_e32 v85, 0, v85, vcc
	v_lshlrev_b64 v[2:3], 5, v[2:3]
	s_ashr_i32 s15, s14, 31
	v_mul_f32_e32 v86, 0x3f317217, v84
	v_fma_f32 v86, v84, s2, -v86
	v_fmac_f32_e32 v86, 0x3377d1cf, v84
	s_mov_b32 s2, 0x7f800000
	v_fmac_f32_e32 v86, 0x3f317217, v84
	v_cmp_lt_f32_e64 vcc, |v84|, s2
	v_readlane_b32 s2, v255, 3
	v_readlane_b32 s3, v255, 4
	v_cndmask_b32_e32 v84, v84, v86, vcc
	v_sub_f32_e32 v84, v84, v85
	v_lshl_add_u64 v[2:3], s[2:3], 0, v[2:3]
	v_fmac_f32_e32 v84, 0x3f317218, v0
	v_lshl_add_u64 v[2:3], s[14:15], 2, v[2:3]
	global_store_dword v[2:3], v84, off
